# moe_cvt: no redundant tail loads (loads stop after the last item; the tail finishes use exact counted waits), otherwise v34
# baseline (speedup 1.0000x reference)
.Lcvt_run:
	s_mov_b32 s31, s10
	s_cmp_eq_u32 s31, 0
	s_cbranch_scc1 .Lcvt_noload_1
	global_load_dwordx4 v[2:5], v98, s[6:7]
	global_load_dwordx4 v[6:9], v99, s[6:7]
	global_load_dwordx4 v[10:13], v100, s[6:7]
	global_load_dwordx4 v[14:17], v101, s[6:7]
	global_load_dwordx4 v[18:21], v102, s[6:7]
	global_load_dwordx4 v[22:25], v103, s[6:7]
	global_load_dwordx4 v[26:29], v104, s[6:7]
	global_load_dwordx4 v[30:33], v105, s[6:7]
	s_add_u32 s6, s6, s13
	s_addc_u32 s7, s7, 0
	s_add_i32 s31, s31, -1
.Lcvt_noload_1:
	s_cmp_eq_u32 s31, 0
	s_cbranch_scc1 .Lcvt_noload_2
	global_load_dwordx4 v[34:37], v98, s[6:7]
	global_load_dwordx4 v[38:41], v99, s[6:7]
	global_load_dwordx4 v[42:45], v100, s[6:7]
	global_load_dwordx4 v[46:49], v101, s[6:7]
	global_load_dwordx4 v[50:53], v102, s[6:7]
	global_load_dwordx4 v[54:57], v103, s[6:7]
	global_load_dwordx4 v[58:61], v104, s[6:7]
	global_load_dwordx4 v[62:65], v105, s[6:7]
	s_add_u32 s6, s6, s13
	s_addc_u32 s7, s7, 0
	s_add_i32 s31, s31, -1
.Lcvt_noload_2:
	s_cmp_eq_u32 s31, 0
	s_cbranch_scc1 .Lcvt_noload_3
	global_load_dwordx4 v[66:69], v98, s[6:7]
	global_load_dwordx4 v[70:73], v99, s[6:7]
	global_load_dwordx4 v[74:77], v100, s[6:7]
	global_load_dwordx4 v[78:81], v101, s[6:7]
	global_load_dwordx4 v[82:85], v102, s[6:7]
	global_load_dwordx4 v[86:89], v103, s[6:7]
	global_load_dwordx4 v[90:93], v104, s[6:7]
	global_load_dwordx4 v[94:97], v105, s[6:7]
	s_add_u32 s6, s6, s13
	s_addc_u32 s7, s7, 0
	s_add_i32 s31, s31, -1
.Lcvt_noload_3:
	s_cmp_eq_u32 s31, 0
	s_cbranch_scc1 .Lcvt_noload_4
	global_load_dwordx4 v[124:127], v98, s[6:7]
	global_load_dwordx4 v[128:131], v99, s[6:7]
	global_load_dwordx4 v[132:135], v100, s[6:7]
	global_load_dwordx4 v[136:139], v101, s[6:7]
	global_load_dwordx4 v[140:143], v102, s[6:7]
	global_load_dwordx4 v[144:147], v103, s[6:7]
	global_load_dwordx4 v[148:151], v104, s[6:7]
	global_load_dwordx4 v[152:155], v105, s[6:7]
	s_add_u32 s6, s6, s13
	s_addc_u32 s7, s7, 0
	s_add_i32 s31, s31, -1
.Lcvt_noload_4:
.Lcvt_loop:
	s_cmp_eq_u32 s31, 0
	s_cbranch_scc1 .Lcvt_noload_5
	global_load_dwordx4 v[156:159], v98, s[6:7]
	global_load_dwordx4 v[160:163], v99, s[6:7]
	global_load_dwordx4 v[164:167], v100, s[6:7]
	global_load_dwordx4 v[168:171], v101, s[6:7]
	global_load_dwordx4 v[172:175], v102, s[6:7]
	global_load_dwordx4 v[176:179], v103, s[6:7]
	global_load_dwordx4 v[180:183], v104, s[6:7]
	global_load_dwordx4 v[184:187], v105, s[6:7]
	s_add_u32 s6, s6, s13
	s_addc_u32 s7, s7, 0
	s_add_i32 s31, s31, -1
.Lcvt_noload_5:
	s_cmp_eq_u32 s10, 1
	s_cbranch_scc1 .Lcvt_w0_1
	s_cmp_eq_u32 s10, 2
	s_cbranch_scc1 .Lcvt_w1_1
	s_cmp_eq_u32 s10, 3
	s_cbranch_scc1 .Lcvt_w2_1
	s_cmp_eq_u32 s10, 4
	s_cbranch_scc1 .Lcvt_w3_1
	s_waitcnt vmcnt(32)
	s_branch .Lcvt_wd_1
.Lcvt_w3_1:
	s_waitcnt vmcnt(24)
	s_branch .Lcvt_wd_1
.Lcvt_w2_1:
	s_waitcnt vmcnt(16)
	s_branch .Lcvt_wd_1
.Lcvt_w1_1:
	s_waitcnt vmcnt(8)
	s_branch .Lcvt_wd_1

.Lcvt_wd_1:
	ds_write2_b32 v106, v2, v3 offset1:1
	ds_write2_b32 v106, v4, v5 offset0:2 offset1:3
	ds_write2_b32 v107, v6, v7 offset1:1
	ds_write2_b32 v107, v8, v9 offset0:2 offset1:3
	ds_write2_b32 v108, v10, v11 offset1:1
	ds_write2_b32 v108, v12, v13 offset0:2 offset1:3
	ds_write2_b32 v109, v14, v15 offset1:1
	ds_write2_b32 v109, v16, v17 offset0:2 offset1:3
	ds_write2_b32 v110, v18, v19 offset1:1
	ds_write2_b32 v110, v20, v21 offset0:2 offset1:3
	ds_write2_b32 v111, v22, v23 offset1:1
	ds_write2_b32 v111, v24, v25 offset0:2 offset1:3
	ds_write2_b32 v112, v26, v27 offset1:1
	ds_write2_b32 v112, v28, v29 offset0:2 offset1:3
	ds_write2_b32 v113, v30, v31 offset1:1
	ds_write2_b32 v113, v32, v33 offset0:2 offset1:3
	s_waitcnt lgkmcnt(0)
	ds_read2_b32 v[2:3], v114 offset1:33
	ds_read2_b32 v[4:5], v114 offset0:66 offset1:99
	ds_read2_b32 v[6:7], v114 offset0:132 offset1:165
	ds_read2_b32 v[8:9], v114 offset0:198 offset1:231
	ds_read2_b32 v[10:11], v114 offset0:8 offset1:41
	ds_read2_b32 v[12:13], v114 offset0:74 offset1:107
	ds_read2_b32 v[14:15], v114 offset0:140 offset1:173
	ds_read2_b32 v[16:17], v114 offset0:206 offset1:239
	ds_read2_b32 v[18:19], v114 offset0:16 offset1:49
	ds_read2_b32 v[20:21], v114 offset0:82 offset1:115
	ds_read2_b32 v[22:23], v114 offset0:148 offset1:181
	ds_read2_b32 v[24:25], v114 offset0:214 offset1:247
	ds_read2_b32 v[26:27], v114 offset0:24 offset1:57
	ds_read2_b32 v[28:29], v114 offset0:90 offset1:123
	ds_read2_b32 v[30:31], v114 offset0:156 offset1:189
	ds_read2_b32 v[32:33], v114 offset0:222 offset1:255
	s_waitcnt lgkmcnt(12)
	v_pk_mul_f32 v[2:3], v[2:3], s[26:27] op_sel_hi:[1,0]
	v_pk_mul_f32 v[4:5], v[4:5], s[26:27] op_sel_hi:[1,0]
	v_pk_mul_f32 v[6:7], v[6:7], s[26:27] op_sel_hi:[1,0]
	v_pk_mul_f32 v[8:9], v[8:9], s[26:27] op_sel_hi:[1,0]
	v_cvt_pk_fp8_f32 v2, v2, v3
	v_cvt_pk_fp8_f32 v3, v6, v7
	v_cvt_pk_fp8_f32 v2, v4, v5 op_sel:[0,0,1]
	v_cvt_pk_fp8_f32 v3, v8, v9 op_sel:[0,0,1]
	s_nop 1
	global_store_dwordx2 v115, v[2:3], s[8:9]
	s_waitcnt lgkmcnt(8)
	v_pk_mul_f32 v[10:11], v[10:11], s[26:27] op_sel_hi:[1,0]
	v_pk_mul_f32 v[12:13], v[12:13], s[26:27] op_sel_hi:[1,0]
	v_pk_mul_f32 v[14:15], v[14:15], s[26:27] op_sel_hi:[1,0]
	v_pk_mul_f32 v[16:17], v[16:17], s[26:27] op_sel_hi:[1,0]
	v_cvt_pk_fp8_f32 v10, v10, v11
	v_cvt_pk_fp8_f32 v11, v14, v15
	v_cvt_pk_fp8_f32 v10, v12, v13 op_sel:[0,0,1]
	v_cvt_pk_fp8_f32 v11, v16, v17 op_sel:[0,0,1]
	s_nop 1
	global_store_dwordx2 v116, v[10:11], s[8:9]
	s_waitcnt lgkmcnt(4)
	v_pk_mul_f32 v[18:19], v[18:19], s[26:27] op_sel_hi:[1,0]
	v_pk_mul_f32 v[20:21], v[20:21], s[26:27] op_sel_hi:[1,0]
	v_pk_mul_f32 v[22:23], v[22:23], s[26:27] op_sel_hi:[1,0]
	v_pk_mul_f32 v[24:25], v[24:25], s[26:27] op_sel_hi:[1,0]
	v_cvt_pk_fp8_f32 v18, v18, v19
	v_cvt_pk_fp8_f32 v19, v22, v23
	v_cvt_pk_fp8_f32 v18, v20, v21 op_sel:[0,0,1]
	v_cvt_pk_fp8_f32 v19, v24, v25 op_sel:[0,0,1]
	s_nop 1
	global_store_dwordx2 v117, v[18:19], s[8:9]
	s_waitcnt lgkmcnt(0)
	v_pk_mul_f32 v[26:27], v[26:27], s[26:27] op_sel_hi:[1,0]
	v_pk_mul_f32 v[28:29], v[28:29], s[26:27] op_sel_hi:[1,0]
	v_pk_mul_f32 v[30:31], v[30:31], s[26:27] op_sel_hi:[1,0]
	v_pk_mul_f32 v[32:33], v[32:33], s[26:27] op_sel_hi:[1,0]
	v_cvt_pk_fp8_f32 v26, v26, v27
	v_cvt_pk_fp8_f32 v27, v30, v31
	v_cvt_pk_fp8_f32 v26, v28, v29 op_sel:[0,0,1]
	v_cvt_pk_fp8_f32 v27, v32, v33 op_sel:[0,0,1]
	s_nop 1
	global_store_dwordx2 v118, v[26:27], s[8:9]
	s_add_u32 s8, s8, s23
	s_addc_u32 s9, s9, 0
	s_add_i32 s10, s10, -1
	s_cmp_eq_u32 s10, 0
	s_cbranch_scc1 .Lcvt_phase_done
	s_cmp_eq_u32 s31, 0
	s_cbranch_scc1 .Lcvt_noload_6
	global_load_dwordx4 v[2:5], v98, s[6:7]
	global_load_dwordx4 v[6:9], v99, s[6:7]
	global_load_dwordx4 v[10:13], v100, s[6:7]
	global_load_dwordx4 v[14:17], v101, s[6:7]
	global_load_dwordx4 v[18:21], v102, s[6:7]
	global_load_dwordx4 v[22:25], v103, s[6:7]
	global_load_dwordx4 v[26:29], v104, s[6:7]
	global_load_dwordx4 v[30:33], v105, s[6:7]
	s_add_u32 s6, s6, s13
	s_addc_u32 s7, s7, 0
	s_add_i32 s31, s31, -1

.Lcvt_wd_2:
	ds_write2_b32 v106, v34, v35 offset1:1
	ds_write2_b32 v106, v36, v37 offset0:2 offset1:3
	ds_write2_b32 v107, v38, v39 offset1:1
	ds_write2_b32 v107, v40, v41 offset0:2 offset1:3
	ds_write2_b32 v108, v42, v43 offset1:1
	ds_write2_b32 v108, v44, v45 offset0:2 offset1:3
	ds_write2_b32 v109, v46, v47 offset1:1
	ds_write2_b32 v109, v48, v49 offset0:2 offset1:3
	ds_write2_b32 v110, v50, v51 offset1:1
	ds_write2_b32 v110, v52, v53 offset0:2 offset1:3
	ds_write2_b32 v111, v54, v55 offset1:1
	ds_write2_b32 v111, v56, v57 offset0:2 offset1:3
	ds_write2_b32 v112, v58, v59 offset1:1
	ds_write2_b32 v112, v60, v61 offset0:2 offset1:3
	ds_write2_b32 v113, v62, v63 offset1:1
	ds_write2_b32 v113, v64, v65 offset0:2 offset1:3
	s_waitcnt lgkmcnt(0)
	ds_read2_b32 v[34:35], v114 offset1:33
	ds_read2_b32 v[36:37], v114 offset0:66 offset1:99
	ds_read2_b32 v[38:39], v114 offset0:132 offset1:165
	ds_read2_b32 v[40:41], v114 offset0:198 offset1:231
	ds_read2_b32 v[42:43], v114 offset0:8 offset1:41
	ds_read2_b32 v[44:45], v114 offset0:74 offset1:107
	ds_read2_b32 v[46:47], v114 offset0:140 offset1:173
	ds_read2_b32 v[48:49], v114 offset0:206 offset1:239
	ds_read2_b32 v[50:51], v114 offset0:16 offset1:49
	ds_read2_b32 v[52:53], v114 offset0:82 offset1:115
	ds_read2_b32 v[54:55], v114 offset0:148 offset1:181
	ds_read2_b32 v[56:57], v114 offset0:214 offset1:247
	ds_read2_b32 v[58:59], v114 offset0:24 offset1:57
	ds_read2_b32 v[60:61], v114 offset0:90 offset1:123
	ds_read2_b32 v[62:63], v114 offset0:156 offset1:189
	ds_read2_b32 v[64:65], v114 offset0:222 offset1:255
	s_waitcnt lgkmcnt(12)
	v_pk_mul_f32 v[34:35], v[34:35], s[26:27] op_sel_hi:[1,0]
	v_pk_mul_f32 v[36:37], v[36:37], s[26:27] op_sel_hi:[1,0]
	v_pk_mul_f32 v[38:39], v[38:39], s[26:27] op_sel_hi:[1,0]
	v_pk_mul_f32 v[40:41], v[40:41], s[26:27] op_sel_hi:[1,0]
	v_cvt_pk_fp8_f32 v34, v34, v35
	v_cvt_pk_fp8_f32 v35, v38, v39
	v_cvt_pk_fp8_f32 v34, v36, v37 op_sel:[0,0,1]
	v_cvt_pk_fp8_f32 v35, v40, v41 op_sel:[0,0,1]
	s_nop 1
	global_store_dwordx2 v115, v[34:35], s[8:9]
	s_waitcnt lgkmcnt(8)
	v_pk_mul_f32 v[42:43], v[42:43], s[26:27] op_sel_hi:[1,0]
	v_pk_mul_f32 v[44:45], v[44:45], s[26:27] op_sel_hi:[1,0]
	v_pk_mul_f32 v[46:47], v[46:47], s[26:27] op_sel_hi:[1,0]
	v_pk_mul_f32 v[48:49], v[48:49], s[26:27] op_sel_hi:[1,0]
	v_cvt_pk_fp8_f32 v42, v42, v43
	v_cvt_pk_fp8_f32 v43, v46, v47
	v_cvt_pk_fp8_f32 v42, v44, v45 op_sel:[0,0,1]
	v_cvt_pk_fp8_f32 v43, v48, v49 op_sel:[0,0,1]
	s_nop 1
	global_store_dwordx2 v116, v[42:43], s[8:9]
	s_waitcnt lgkmcnt(4)
	v_pk_mul_f32 v[50:51], v[50:51], s[26:27] op_sel_hi:[1,0]
	v_pk_mul_f32 v[52:53], v[52:53], s[26:27] op_sel_hi:[1,0]
	v_pk_mul_f32 v[54:55], v[54:55], s[26:27] op_sel_hi:[1,0]
	v_pk_mul_f32 v[56:57], v[56:57], s[26:27] op_sel_hi:[1,0]
	v_cvt_pk_fp8_f32 v50, v50, v51
	v_cvt_pk_fp8_f32 v51, v54, v55
	v_cvt_pk_fp8_f32 v50, v52, v53 op_sel:[0,0,1]
	v_cvt_pk_fp8_f32 v51, v56, v57 op_sel:[0,0,1]
	s_nop 1
	global_store_dwordx2 v117, v[50:51], s[8:9]
	s_waitcnt lgkmcnt(0)
	v_pk_mul_f32 v[58:59], v[58:59], s[26:27] op_sel_hi:[1,0]
	v_pk_mul_f32 v[60:61], v[60:61], s[26:27] op_sel_hi:[1,0]
	v_pk_mul_f32 v[62:63], v[62:63], s[26:27] op_sel_hi:[1,0]
	v_pk_mul_f32 v[64:65], v[64:65], s[26:27] op_sel_hi:[1,0]
	v_cvt_pk_fp8_f32 v58, v58, v59
	v_cvt_pk_fp8_f32 v59, v62, v63
	v_cvt_pk_fp8_f32 v58, v60, v61 op_sel:[0,0,1]
	v_cvt_pk_fp8_f32 v59, v64, v65 op_sel:[0,0,1]
	s_nop 1
	global_store_dwordx2 v118, v[58:59], s[8:9]
	s_add_u32 s8, s8, s23
	s_addc_u32 s9, s9, 0
	s_add_i32 s10, s10, -1
	s_cmp_eq_u32 s10, 0
	s_cbranch_scc1 .Lcvt_phase_done
	s_cmp_eq_u32 s31, 0
	s_cbranch_scc1 .Lcvt_noload_7
	global_load_dwordx4 v[34:37], v98, s[6:7]
	global_load_dwordx4 v[38:41], v99, s[6:7]
	global_load_dwordx4 v[42:45], v100, s[6:7]
	global_load_dwordx4 v[46:49], v101, s[6:7]
	global_load_dwordx4 v[50:53], v102, s[6:7]
	global_load_dwordx4 v[54:57], v103, s[6:7]
	global_load_dwordx4 v[58:61], v104, s[6:7]
	global_load_dwordx4 v[62:65], v105, s[6:7]
	s_add_u32 s6, s6, s13
	s_addc_u32 s7, s7, 0
	s_add_i32 s31, s31, -1

.Lcvt_wd_3:
	ds_write2_b32 v106, v66, v67 offset1:1
	ds_write2_b32 v106, v68, v69 offset0:2 offset1:3
	ds_write2_b32 v107, v70, v71 offset1:1
	ds_write2_b32 v107, v72, v73 offset0:2 offset1:3
	ds_write2_b32 v108, v74, v75 offset1:1
	ds_write2_b32 v108, v76, v77 offset0:2 offset1:3
	ds_write2_b32 v109, v78, v79 offset1:1
	ds_write2_b32 v109, v80, v81 offset0:2 offset1:3
	ds_write2_b32 v110, v82, v83 offset1:1
	ds_write2_b32 v110, v84, v85 offset0:2 offset1:3
	ds_write2_b32 v111, v86, v87 offset1:1
	ds_write2_b32 v111, v88, v89 offset0:2 offset1:3
	ds_write2_b32 v112, v90, v91 offset1:1
	ds_write2_b32 v112, v92, v93 offset0:2 offset1:3
	ds_write2_b32 v113, v94, v95 offset1:1
	ds_write2_b32 v113, v96, v97 offset0:2 offset1:3
	s_waitcnt lgkmcnt(0)
	ds_read2_b32 v[66:67], v114 offset1:33
	ds_read2_b32 v[68:69], v114 offset0:66 offset1:99
	ds_read2_b32 v[70:71], v114 offset0:132 offset1:165
	ds_read2_b32 v[72:73], v114 offset0:198 offset1:231
	ds_read2_b32 v[74:75], v114 offset0:8 offset1:41
	ds_read2_b32 v[76:77], v114 offset0:74 offset1:107
	ds_read2_b32 v[78:79], v114 offset0:140 offset1:173
	ds_read2_b32 v[80:81], v114 offset0:206 offset1:239
	ds_read2_b32 v[82:83], v114 offset0:16 offset1:49
	ds_read2_b32 v[84:85], v114 offset0:82 offset1:115
	ds_read2_b32 v[86:87], v114 offset0:148 offset1:181
	ds_read2_b32 v[88:89], v114 offset0:214 offset1:247
	ds_read2_b32 v[90:91], v114 offset0:24 offset1:57
	ds_read2_b32 v[92:93], v114 offset0:90 offset1:123
	ds_read2_b32 v[94:95], v114 offset0:156 offset1:189
	ds_read2_b32 v[96:97], v114 offset0:222 offset1:255
	s_waitcnt lgkmcnt(12)
	v_pk_mul_f32 v[66:67], v[66:67], s[26:27] op_sel_hi:[1,0]
	v_pk_mul_f32 v[68:69], v[68:69], s[26:27] op_sel_hi:[1,0]
	v_pk_mul_f32 v[70:71], v[70:71], s[26:27] op_sel_hi:[1,0]
	v_pk_mul_f32 v[72:73], v[72:73], s[26:27] op_sel_hi:[1,0]
	v_cvt_pk_fp8_f32 v66, v66, v67
	v_cvt_pk_fp8_f32 v67, v70, v71
	v_cvt_pk_fp8_f32 v66, v68, v69 op_sel:[0,0,1]
	v_cvt_pk_fp8_f32 v67, v72, v73 op_sel:[0,0,1]
	s_nop 1
	global_store_dwordx2 v115, v[66:67], s[8:9]
	s_waitcnt lgkmcnt(8)
	v_pk_mul_f32 v[74:75], v[74:75], s[26:27] op_sel_hi:[1,0]
	v_pk_mul_f32 v[76:77], v[76:77], s[26:27] op_sel_hi:[1,0]
	v_pk_mul_f32 v[78:79], v[78:79], s[26:27] op_sel_hi:[1,0]
	v_pk_mul_f32 v[80:81], v[80:81], s[26:27] op_sel_hi:[1,0]
	v_cvt_pk_fp8_f32 v74, v74, v75
	v_cvt_pk_fp8_f32 v75, v78, v79
	v_cvt_pk_fp8_f32 v74, v76, v77 op_sel:[0,0,1]
	v_cvt_pk_fp8_f32 v75, v80, v81 op_sel:[0,0,1]
	s_nop 1
	global_store_dwordx2 v116, v[74:75], s[8:9]
	s_waitcnt lgkmcnt(4)
	v_pk_mul_f32 v[82:83], v[82:83], s[26:27] op_sel_hi:[1,0]
	v_pk_mul_f32 v[84:85], v[84:85], s[26:27] op_sel_hi:[1,0]
	v_pk_mul_f32 v[86:87], v[86:87], s[26:27] op_sel_hi:[1,0]
	v_pk_mul_f32 v[88:89], v[88:89], s[26:27] op_sel_hi:[1,0]
	v_cvt_pk_fp8_f32 v82, v82, v83
	v_cvt_pk_fp8_f32 v83, v86, v87
	v_cvt_pk_fp8_f32 v82, v84, v85 op_sel:[0,0,1]
	v_cvt_pk_fp8_f32 v83, v88, v89 op_sel:[0,0,1]
	s_nop 1
	global_store_dwordx2 v117, v[82:83], s[8:9]
	s_waitcnt lgkmcnt(0)
	v_pk_mul_f32 v[90:91], v[90:91], s[26:27] op_sel_hi:[1,0]
	v_pk_mul_f32 v[92:93], v[92:93], s[26:27] op_sel_hi:[1,0]
	v_pk_mul_f32 v[94:95], v[94:95], s[26:27] op_sel_hi:[1,0]
	v_pk_mul_f32 v[96:97], v[96:97], s[26:27] op_sel_hi:[1,0]
	v_cvt_pk_fp8_f32 v90, v90, v91
	v_cvt_pk_fp8_f32 v91, v94, v95
	v_cvt_pk_fp8_f32 v90, v92, v93 op_sel:[0,0,1]
	v_cvt_pk_fp8_f32 v91, v96, v97 op_sel:[0,0,1]
	s_nop 1
	global_store_dwordx2 v118, v[90:91], s[8:9]
	s_add_u32 s8, s8, s23
	s_addc_u32 s9, s9, 0
	s_add_i32 s10, s10, -1
	s_cmp_eq_u32 s10, 0
	s_cbranch_scc1 .Lcvt_phase_done
	s_cmp_eq_u32 s31, 0
	s_cbranch_scc1 .Lcvt_noload_8
	global_load_dwordx4 v[66:69], v98, s[6:7]
	global_load_dwordx4 v[70:73], v99, s[6:7]
	global_load_dwordx4 v[74:77], v100, s[6:7]
	global_load_dwordx4 v[78:81], v101, s[6:7]
	global_load_dwordx4 v[82:85], v102, s[6:7]
	global_load_dwordx4 v[86:89], v103, s[6:7]
	global_load_dwordx4 v[90:93], v104, s[6:7]
	global_load_dwordx4 v[94:97], v105, s[6:7]
	s_add_u32 s6, s6, s13
	s_addc_u32 s7, s7, 0
	s_add_i32 s31, s31, -1

.Lcvt_wd_4:
	ds_write2_b32 v106, v124, v125 offset1:1
	ds_write2_b32 v106, v126, v127 offset0:2 offset1:3
	ds_write2_b32 v107, v128, v129 offset1:1
	ds_write2_b32 v107, v130, v131 offset0:2 offset1:3
	ds_write2_b32 v108, v132, v133 offset1:1
	ds_write2_b32 v108, v134, v135 offset0:2 offset1:3
	ds_write2_b32 v109, v136, v137 offset1:1
	ds_write2_b32 v109, v138, v139 offset0:2 offset1:3
	ds_write2_b32 v110, v140, v141 offset1:1
	ds_write2_b32 v110, v142, v143 offset0:2 offset1:3
	ds_write2_b32 v111, v144, v145 offset1:1
	ds_write2_b32 v111, v146, v147 offset0:2 offset1:3
	ds_write2_b32 v112, v148, v149 offset1:1
	ds_write2_b32 v112, v150, v151 offset0:2 offset1:3
	ds_write2_b32 v113, v152, v153 offset1:1
	ds_write2_b32 v113, v154, v155 offset0:2 offset1:3
	s_waitcnt lgkmcnt(0)
	ds_read2_b32 v[124:125], v114 offset1:33
	ds_read2_b32 v[126:127], v114 offset0:66 offset1:99
	ds_read2_b32 v[128:129], v114 offset0:132 offset1:165
	ds_read2_b32 v[130:131], v114 offset0:198 offset1:231
	ds_read2_b32 v[132:133], v114 offset0:8 offset1:41
	ds_read2_b32 v[134:135], v114 offset0:74 offset1:107
	ds_read2_b32 v[136:137], v114 offset0:140 offset1:173
	ds_read2_b32 v[138:139], v114 offset0:206 offset1:239
	ds_read2_b32 v[140:141], v114 offset0:16 offset1:49
	ds_read2_b32 v[142:143], v114 offset0:82 offset1:115
	ds_read2_b32 v[144:145], v114 offset0:148 offset1:181
	ds_read2_b32 v[146:147], v114 offset0:214 offset1:247
	ds_read2_b32 v[148:149], v114 offset0:24 offset1:57
	ds_read2_b32 v[150:151], v114 offset0:90 offset1:123
	ds_read2_b32 v[152:153], v114 offset0:156 offset1:189
	ds_read2_b32 v[154:155], v114 offset0:222 offset1:255
	s_waitcnt lgkmcnt(12)
	v_pk_mul_f32 v[124:125], v[124:125], s[26:27] op_sel_hi:[1,0]
	v_pk_mul_f32 v[126:127], v[126:127], s[26:27] op_sel_hi:[1,0]
	v_pk_mul_f32 v[128:129], v[128:129], s[26:27] op_sel_hi:[1,0]
	v_pk_mul_f32 v[130:131], v[130:131], s[26:27] op_sel_hi:[1,0]
	v_cvt_pk_fp8_f32 v124, v124, v125
	v_cvt_pk_fp8_f32 v125, v128, v129
	v_cvt_pk_fp8_f32 v124, v126, v127 op_sel:[0,0,1]
	v_cvt_pk_fp8_f32 v125, v130, v131 op_sel:[0,0,1]
	s_nop 1
	global_store_dwordx2 v115, v[124:125], s[8:9]
	s_waitcnt lgkmcnt(8)
	v_pk_mul_f32 v[132:133], v[132:133], s[26:27] op_sel_hi:[1,0]
	v_pk_mul_f32 v[134:135], v[134:135], s[26:27] op_sel_hi:[1,0]
	v_pk_mul_f32 v[136:137], v[136:137], s[26:27] op_sel_hi:[1,0]
	v_pk_mul_f32 v[138:139], v[138:139], s[26:27] op_sel_hi:[1,0]
	v_cvt_pk_fp8_f32 v132, v132, v133
	v_cvt_pk_fp8_f32 v133, v136, v137
	v_cvt_pk_fp8_f32 v132, v134, v135 op_sel:[0,0,1]
	v_cvt_pk_fp8_f32 v133, v138, v139 op_sel:[0,0,1]
	s_nop 1
	global_store_dwordx2 v116, v[132:133], s[8:9]
	s_waitcnt lgkmcnt(4)
	v_pk_mul_f32 v[140:141], v[140:141], s[26:27] op_sel_hi:[1,0]
	v_pk_mul_f32 v[142:143], v[142:143], s[26:27] op_sel_hi:[1,0]
	v_pk_mul_f32 v[144:145], v[144:145], s[26:27] op_sel_hi:[1,0]
	v_pk_mul_f32 v[146:147], v[146:147], s[26:27] op_sel_hi:[1,0]
	v_cvt_pk_fp8_f32 v140, v140, v141
	v_cvt_pk_fp8_f32 v141, v144, v145
	v_cvt_pk_fp8_f32 v140, v142, v143 op_sel:[0,0,1]
	v_cvt_pk_fp8_f32 v141, v146, v147 op_sel:[0,0,1]
	s_nop 1
	global_store_dwordx2 v117, v[140:141], s[8:9]
	s_waitcnt lgkmcnt(0)
	v_pk_mul_f32 v[148:149], v[148:149], s[26:27] op_sel_hi:[1,0]
	v_pk_mul_f32 v[150:151], v[150:151], s[26:27] op_sel_hi:[1,0]
	v_pk_mul_f32 v[152:153], v[152:153], s[26:27] op_sel_hi:[1,0]
	v_pk_mul_f32 v[154:155], v[154:155], s[26:27] op_sel_hi:[1,0]
	v_cvt_pk_fp8_f32 v148, v148, v149
	v_cvt_pk_fp8_f32 v149, v152, v153
	v_cvt_pk_fp8_f32 v148, v150, v151 op_sel:[0,0,1]
	v_cvt_pk_fp8_f32 v149, v154, v155 op_sel:[0,0,1]
	s_nop 1
	global_store_dwordx2 v118, v[148:149], s[8:9]
	s_add_u32 s8, s8, s23
	s_addc_u32 s9, s9, 0
	s_add_i32 s10, s10, -1
	s_cmp_eq_u32 s10, 0
	s_cbranch_scc1 .Lcvt_phase_done
	s_cmp_eq_u32 s31, 0
	s_cbranch_scc1 .Lcvt_noload_9
	global_load_dwordx4 v[124:127], v98, s[6:7]
	global_load_dwordx4 v[128:131], v99, s[6:7]
	global_load_dwordx4 v[132:135], v100, s[6:7]
	global_load_dwordx4 v[136:139], v101, s[6:7]
	global_load_dwordx4 v[140:143], v102, s[6:7]
	global_load_dwordx4 v[144:147], v103, s[6:7]
	global_load_dwordx4 v[148:151], v104, s[6:7]
	global_load_dwordx4 v[152:155], v105, s[6:7]
	s_add_u32 s6, s6, s13
	s_addc_u32 s7, s7, 0
	s_add_i32 s31, s31, -1

.Lcvt_wd_5:
	ds_write2_b32 v106, v156, v157 offset1:1
	ds_write2_b32 v106, v158, v159 offset0:2 offset1:3
	ds_write2_b32 v107, v160, v161 offset1:1
	ds_write2_b32 v107, v162, v163 offset0:2 offset1:3
	ds_write2_b32 v108, v164, v165 offset1:1
	ds_write2_b32 v108, v166, v167 offset0:2 offset1:3
	ds_write2_b32 v109, v168, v169 offset1:1
	ds_write2_b32 v109, v170, v171 offset0:2 offset1:3
	ds_write2_b32 v110, v172, v173 offset1:1
	ds_write2_b32 v110, v174, v175 offset0:2 offset1:3
	ds_write2_b32 v111, v176, v177 offset1:1
	ds_write2_b32 v111, v178, v179 offset0:2 offset1:3
	ds_write2_b32 v112, v180, v181 offset1:1
	ds_write2_b32 v112, v182, v183 offset0:2 offset1:3
	ds_write2_b32 v113, v184, v185 offset1:1
	ds_write2_b32 v113, v186, v187 offset0:2 offset1:3
	s_waitcnt lgkmcnt(0)
	ds_read2_b32 v[156:157], v114 offset1:33
	ds_read2_b32 v[158:159], v114 offset0:66 offset1:99
	ds_read2_b32 v[160:161], v114 offset0:132 offset1:165
	ds_read2_b32 v[162:163], v114 offset0:198 offset1:231
	ds_read2_b32 v[164:165], v114 offset0:8 offset1:41
	ds_read2_b32 v[166:167], v114 offset0:74 offset1:107
	ds_read2_b32 v[168:169], v114 offset0:140 offset1:173
	ds_read2_b32 v[170:171], v114 offset0:206 offset1:239
	ds_read2_b32 v[172:173], v114 offset0:16 offset1:49
	ds_read2_b32 v[174:175], v114 offset0:82 offset1:115
	ds_read2_b32 v[176:177], v114 offset0:148 offset1:181
	ds_read2_b32 v[178:179], v114 offset0:214 offset1:247
	ds_read2_b32 v[180:181], v114 offset0:24 offset1:57
	ds_read2_b32 v[182:183], v114 offset0:90 offset1:123
	ds_read2_b32 v[184:185], v114 offset0:156 offset1:189
	ds_read2_b32 v[186:187], v114 offset0:222 offset1:255
	s_waitcnt lgkmcnt(12)
	v_pk_mul_f32 v[156:157], v[156:157], s[26:27] op_sel_hi:[1,0]
	v_pk_mul_f32 v[158:159], v[158:159], s[26:27] op_sel_hi:[1,0]
	v_pk_mul_f32 v[160:161], v[160:161], s[26:27] op_sel_hi:[1,0]
	v_pk_mul_f32 v[162:163], v[162:163], s[26:27] op_sel_hi:[1,0]
	v_cvt_pk_fp8_f32 v156, v156, v157
	v_cvt_pk_fp8_f32 v157, v160, v161
	v_cvt_pk_fp8_f32 v156, v158, v159 op_sel:[0,0,1]
	v_cvt_pk_fp8_f32 v157, v162, v163 op_sel:[0,0,1]
	s_nop 1
	global_store_dwordx2 v115, v[156:157], s[8:9]
	s_waitcnt lgkmcnt(8)
	v_pk_mul_f32 v[164:165], v[164:165], s[26:27] op_sel_hi:[1,0]
	v_pk_mul_f32 v[166:167], v[166:167], s[26:27] op_sel_hi:[1,0]
	v_pk_mul_f32 v[168:169], v[168:169], s[26:27] op_sel_hi:[1,0]
	v_pk_mul_f32 v[170:171], v[170:171], s[26:27] op_sel_hi:[1,0]
	v_cvt_pk_fp8_f32 v164, v164, v165
	v_cvt_pk_fp8_f32 v165, v168, v169
	v_cvt_pk_fp8_f32 v164, v166, v167 op_sel:[0,0,1]
	v_cvt_pk_fp8_f32 v165, v170, v171 op_sel:[0,0,1]
	s_nop 1
	global_store_dwordx2 v116, v[164:165], s[8:9]
	s_waitcnt lgkmcnt(4)
	v_pk_mul_f32 v[172:173], v[172:173], s[26:27] op_sel_hi:[1,0]
	v_pk_mul_f32 v[174:175], v[174:175], s[26:27] op_sel_hi:[1,0]
	v_pk_mul_f32 v[176:177], v[176:177], s[26:27] op_sel_hi:[1,0]
	v_pk_mul_f32 v[178:179], v[178:179], s[26:27] op_sel_hi:[1,0]
	v_cvt_pk_fp8_f32 v172, v172, v173
	v_cvt_pk_fp8_f32 v173, v176, v177
	v_cvt_pk_fp8_f32 v172, v174, v175 op_sel:[0,0,1]
	v_cvt_pk_fp8_f32 v173, v178, v179 op_sel:[0,0,1]
	s_nop 1
	global_store_dwordx2 v117, v[172:173], s[8:9]
	s_waitcnt lgkmcnt(0)
	v_pk_mul_f32 v[180:181], v[180:181], s[26:27] op_sel_hi:[1,0]
	v_pk_mul_f32 v[182:183], v[182:183], s[26:27] op_sel_hi:[1,0]
	v_pk_mul_f32 v[184:185], v[184:185], s[26:27] op_sel_hi:[1,0]
	v_pk_mul_f32 v[186:187], v[186:187], s[26:27] op_sel_hi:[1,0]
	v_cvt_pk_fp8_f32 v180, v180, v181
	v_cvt_pk_fp8_f32 v181, v184, v185
	v_cvt_pk_fp8_f32 v180, v182, v183 op_sel:[0,0,1]
	v_cvt_pk_fp8_f32 v181, v186, v187 op_sel:[0,0,1]
	s_nop 1
	global_store_dwordx2 v118, v[180:181], s[8:9]
	s_add_u32 s8, s8, s23
	s_addc_u32 s9, s9, 0
	s_add_i32 s10, s10, -1
	s_cmp_eq_u32 s10, 0
	s_cbranch_scc1 .Lcvt_phase_done
	s_branch .Lcvt_loop
